# MLA loop: two barriers per key tile, waves 4-7 run half a tile behind waves 0-3 (QK+softmax of one wave beside PV of its SIMD partner); K pieces issued in the QK segment, V pieces in the PV segment
# baseline (speedup 1.0000x reference)
; template <bool MLA>
; __device__ __forceinline__ void attn_unit(char* lds, int h, int qb, const bf16_t* Qp, int ldq, const bf16_t* Kp, int ldk, const bf16_t* KRp, const bf16_t* Vp, int ldv,
;                                           unsigned char* Op, int ldo, const float* KMp, const float* rel_bias) {
;     ...
;     for (int i = 0; i < 2; ++i) { const int pc = wid * 2 + i;
;         { const int row = pc * 4 + (lane >> 4), colB = ((lane & 15) * 16) ^ ((row & 7) << 4); offKn[i] = (unsigned)(row * ldk + (colB >> 1)); }
;         { const int sub = pc * 2 + (lane >> 5), kk = (sub >> 2) * 8 + ((lane & 31) >> 2), c = (sub & 3) * 32 + (lane & 3) * 8; const int k = (kk & ~0xC) | ((kk & 4) << 1) | ((kk & 8) >> 1);
;           offV[i] = (unsigned)(k * ldv + c); } }
;     { const int row = wid * 8 + (lane >> 3), colB = ((lane & 7) * 16) ^ ((row & 7) << 4); offKr = (unsigned)(row * 64 + (colB >> 1)); }
;     ...
;     A_ISSUE(0, 0);
;     bf16x8 qr[NQ];
;     { const bf16_t* qrow = Qp + (size_t)qpos * ldq;
; #pragma unroll
;       for (int d0 = 0; d0 < NQ; ++d0) qr[d0] = *(const bf16x8*)(qrow + d0 * 16 + hi * 8); }
;     unsigned mysel = 0u;
;     if constexpr (!MLA) {
;         if (tid <= 128) { const int n = tid; int bk; if (n < 16) bk = n; else { const float v = logf((float)n * (1.0f / 16.0f)) / logf(8.0f) * 16.0f; bk = 16 + (int)v; if (bk > 31) bk = 31; }
;             bt_l[tid] = rel_bias[bk * 8 + h] * (1.0f / SCALE); }
;         for (int i = tid; i < 16 * 128; i += 512) km_l[i] = KMp[i] + KMp[i + 65536];
;         __syncthreads();
;         { const int row = tid >> 1, half = tid & 1;
;           unsigned mask;
;           if (qb <= 3) mask = (1u << qb) - 1u;
;           else { const bf16_t* qrow = Qp + (size_t)(q0 + row) * ldq + half * 64;
;               u32x4 qv[8];
; #pragma unroll
;               for (int c = 0; c < 8; ++c) qv[c] = *(const u32x4*)(qrow + c * 8);
;               float v0 = NEG, v1 = NEG, v2 = NEG; int i0 = 0, i1 = 0, i2 = 0;
; #pragma unroll 1
;               for (int n = 0; n < qb; ++n) { const float* kp = km_l + n * 128 + half * 64; float x = 0.f;
; #pragma unroll
;                   for (int c = 0; c < 8; ++c) { const f32x4 k0 = *(const f32x4*)(kp + c * 8), k1 = *(const f32x4*)(kp + c * 8 + 4);
.LBB0_1381:
	s_or_b64 exec, exec, s[42:43]
	s_waitcnt lgkmcnt(0)
	s_barrier
	ds_read_b32 v2, v161
	s_mov_b64 s[42:43], -1
	s_waitcnt lgkmcnt(0)
	s_barrier
	v_cmp_lt_i32_e32 vcc, s16, v2
	v_readfirstlane_b32 s10, v2
	s_cbranch_vccnz .LBB0_1376
	s_ashr_i32 s22, s10, 5
	s_and_b32 s27, s10, 7
	s_lshl_b32 s10, s10, 9
	s_and_b32 s10, s10, 0x3000
	s_sub_i32 s23, 15, s22
	s_mul_i32 s42, s10, 0xc00
	s_add_u32 s42, s30, s42
	s_addc_u32 s43, s31, 0
	s_mul_i32 s44, s27, 0x180
	s_add_u32 s46, s42, s44
	s_addc_u32 s47, s43, 0
	s_lshl_b32 s43, s10, 11
	s_lshl_b32 s42, s10, 12
	s_add_u32 s42, s12, s42
	s_addc_u32 s45, s13, 0
	s_lshl_b32 s44, s27, 9
	s_add_u32 s44, s42, s44
	s_addc_u32 s45, s45, 0
	s_lshl_b32 s10, s10, 7
	s_add_u32 s50, s75, s10
	v_readfirstlane_b32 s10, v0
	s_addc_u32 s51, s76, 0
	s_lshr_b32 s49, s10, 6
	s_lshl_b32 s48, s49, 3
	s_lshr_b32 s53, s10, 4
	v_bitop3_b32 v2, s48, v162, v187 bitop3:0xc8
	s_and_b32 s53, s53, 4
	v_or3_b32 v2, v2, s53, v190
	v_lshl_or_b32 v3, v2, 11, v188
	v_or_b32_e32 v2, s48, v186
	v_lshl_or_b32 v2, v2, 11, v191
	v_or_b32_e32 v4, s48, v192
	s_lshl_b32 s48, s49, 11
	v_lshlrev_b32_e32 v146, 1, v2
	s_add_i32 s48, s48, 0
	v_lshl_add_u64 v[6:7], s[44:45], 0, v[146:147]
	s_add_i32 m0, s48, 0x8000
	v_mov_b32_e32 v146, v3
	global_load_lds_dwordx4 v[6:7], off
	v_lshl_add_u64 v[6:7], v[146:147], 1, s[44:45]
	v_lshl_or_b32 v4, v4, 11, v193
	v_lshl_add_u64 v[8:9], v[6:7], 0, s[38:39]
	s_mov_b32 m0, s48
	v_lshl_add_u64 v[6:7], v[6:7], 0, s[40:41]
	global_load_lds_dwordx4 v[8:9], off
	v_lshlrev_b32_e32 v8, 1, v4
	v_mov_b32_e32 v9, v147
	v_lshl_add_u64 v[8:9], s[44:45], 0, v[8:9]
	s_add_i32 m0, s48, 0x8400
	s_lshl_b32 s42, s23, 8
	global_load_lds_dwordx4 v[8:9], off
	s_add_i32 m0, s48, 0x400
	s_lshl_b32 s52, s49, 5
	global_load_lds_dwordx4 v[6:7], off
	v_lshl_or_b32 v6, s49, 9, v158
	s_lshl_b32 s49, s49, 10
	s_add_i32 s42, s52, s42
	v_mov_b32_e32 v7, v147
	s_add_i32 s49, s49, 0
	v_or_b32_e32 v5, s42, v168
	v_lshl_add_u64 v[148:149], v[6:7], 1, s[50:51]
	s_add_i32 s49, s49, 0x10000
	v_mov_b64_e32 v[6:7], s[46:47]
	s_mov_b32 m0, s49
	v_mad_u64_u32 v[6:7], s[46:47], v5, s17, v[6:7]
	v_mov_b32_e32 v173, v147
	global_load_lds_dwordx4 v[148:149], off
	v_lshl_add_u64 v[6:7], v[6:7], 0, v[172:173]
	global_load_dwordx4 v[98:101], v[6:7], off
	global_load_dwordx4 v[102:105], v[6:7], off offset:32
	global_load_dwordx4 v[106:109], v[6:7], off offset:64
	global_load_dwordx4 v[110:113], v[6:7], off offset:96
	global_load_dwordx4 v[114:117], v[6:7], off offset:128
	global_load_dwordx4 v[118:121], v[6:7], off offset:160
	global_load_dwordx4 v[122:125], v[6:7], off offset:192
	global_load_dwordx4 v[126:129], v[6:7], off offset:224
	global_load_dwordx4 v[130:133], v[6:7], off offset:256
	global_load_dwordx4 v[134:137], v[6:7], off offset:288
	global_load_dwordx4 v[138:141], v[6:7], off offset:320
	global_load_dwordx4 v[142:145], v[6:7], off offset:352
	s_and_b32 s10, s10, 0x3fffffc0
	s_lshl_b32 s10, s10, 2
	s_add_i32 s10, s10, 0
	s_add_i32 s10, s10, 0x14000
	v_lshl_add_u32 v167, v165, 2, s10
	s_waitcnt vmcnt(0)
	v_lshl_add_u32 v173, v168, 2, s10
	v_add_u32_e32 v3, s52, v160
	s_lshl_b32 s10, s22, 8
	s_waitcnt vmcnt(0)
	v_mov_b32_e32 v34, v147
	v_mov_b32_e32 v35, v147
	v_mov_b32_e32 v48, v147
	v_mov_b32_e32 v49, v147
	s_lshl_b32 s50, s23, 2
	v_subrev_u32_e32 v174, s10, v3
	v_mov_b32_e32 v36, v147
	v_mov_b32_e32 v37, v147
	v_mov_b32_e32 v38, v147
	v_mov_b32_e32 v39, v147
	v_mov_b32_e32 v40, v147
	v_mov_b32_e32 v41, v147
	v_mov_b32_e32 v42, v147
	v_mov_b32_e32 v43, v147
	v_mov_b32_e32 v44, v147
	v_mov_b32_e32 v45, v147
	v_mov_b32_e32 v46, v147
	v_mov_b32_e32 v47, v147
	v_lshlrev_b32_e32 v176, 1, v2
	v_lshlrev_b32_e32 v177, 1, v4
	v_mov_b64_e32 v[64:65], v[48:49]
	v_mov_b64_e32 v[18:19], v[34:35]
	v_mov_b64_e32 v[2:3], v[34:35]
	s_add_i32 s50, s50, 4
	s_or_b32 s51, s42, 31
	s_mov_b32 s52, 0
	v_mov_b32_e32 v178, 0
	v_mov_b32_e32 v175, 0xf149f2ca
	s_mov_b32 s10, 64
	v_mov_b64_e32 v[62:63], v[46:47]
	v_mov_b64_e32 v[60:61], v[44:45]
	v_mov_b64_e32 v[58:59], v[42:43]
	v_mov_b64_e32 v[56:57], v[40:41]
	v_mov_b64_e32 v[54:55], v[38:39]
	v_mov_b64_e32 v[52:53], v[36:37]
	v_mov_b64_e32 v[50:51], v[34:35]
	v_mov_b64_e32 v[20:21], v[36:37]
	v_mov_b64_e32 v[22:23], v[38:39]
	v_mov_b64_e32 v[24:25], v[40:41]
	v_mov_b64_e32 v[26:27], v[42:43]
	v_mov_b64_e32 v[28:29], v[44:45]
	v_mov_b64_e32 v[30:31], v[46:47]
	v_mov_b64_e32 v[32:33], v[48:49]
	v_mov_b64_e32 v[4:5], v[36:37]
	v_mov_b64_e32 v[6:7], v[38:39]
	v_mov_b64_e32 v[8:9], v[40:41]
	v_mov_b64_e32 v[10:11], v[42:43]
	v_mov_b64_e32 v[12:13], v[44:45]
	v_mov_b64_e32 v[14:15], v[46:47]
	v_mov_b64_e32 v[16:17], v[48:49]
	s_waitcnt lgkmcnt(0)
	s_barrier
	v_readfirstlane_b32 s98, v0
	s_nop 3
	s_bitcmp1_b32 s98, 8
	s_cbranch_scc0 .Lmla_noxb
	s_barrier
.Lmla_noxb:
	s_branch .LBB0_1386
; #define LDS_WAIT() asm volatile("s_waitcnt lgkmcnt(0)" ::: "memory")
; template <bool MLA>
; __device__ __forceinline__ void attn_unit(char* lds, int h, int qb, const bf16_t* Qp, int ldq, const bf16_t* Kp, int ldk, const bf16_t* KRp, const bf16_t* Vp, int ldv,
;                                           unsigned char* Op, int ldo, const float* KMp, const float* rel_bias) {
;     ...
;             if (__any(alpha < 1.f)) { if (hi == 0) al_l[r32] = alpha; LDS_WAIT();
; #pragma unroll
;                 for (int r = 0; r < 16; ++r) { const float a = al_h[CROWC(r)];
; #pragma unroll
;                     for (int d_ = 0; d_ < 4; ++d_) o[d_][r] *= a; } }
;             { const int vb0 = vrb + buf * SHM_V;
;     ...
;               PV_D0(0); PV_D0(1); PV_D0(2); PV_D0(3);
.LBB0_1383:
	s_or_b64 exec, exec, s[46:47]
	s_waitcnt lgkmcnt(0)
	ds_read_b128 v[86:89], v167 offset:224
	ds_read_b128 v[90:93], v167 offset:192
	ds_read_b128 v[94:97], v167 offset:160
	ds_read_b128 v[180:183], v167 offset:128
	s_waitcnt lgkmcnt(0)
	v_pk_mul_f32 v[48:49], v[48:49], v[88:89]
	v_pk_mul_f32 v[44:45], v[44:45], v[92:93]
	v_pk_mul_f32 v[40:41], v[40:41], v[96:97]
	v_pk_mul_f32 v[36:37], v[36:37], v[182:183]
	v_pk_mul_f32 v[46:47], v[46:47], v[86:87]
	v_pk_mul_f32 v[42:43], v[42:43], v[90:91]
	v_pk_mul_f32 v[38:39], v[38:39], v[94:95]
	v_pk_mul_f32 v[34:35], v[34:35], v[180:181]
	v_pk_mul_f32 v[64:65], v[64:65], v[88:89]
	v_pk_mul_f32 v[60:61], v[60:61], v[92:93]
	v_pk_mul_f32 v[56:57], v[56:57], v[96:97]
	v_pk_mul_f32 v[52:53], v[52:53], v[182:183]
	v_pk_mul_f32 v[62:63], v[62:63], v[86:87]
	v_pk_mul_f32 v[58:59], v[58:59], v[90:91]
	v_pk_mul_f32 v[54:55], v[54:55], v[94:95]
	v_pk_mul_f32 v[50:51], v[50:51], v[180:181]
	v_pk_mul_f32 v[32:33], v[32:33], v[88:89]
	v_pk_mul_f32 v[28:29], v[28:29], v[92:93]
	v_pk_mul_f32 v[24:25], v[24:25], v[96:97]
	v_pk_mul_f32 v[20:21], v[20:21], v[182:183]
	v_pk_mul_f32 v[30:31], v[30:31], v[86:87]
	v_pk_mul_f32 v[26:27], v[26:27], v[90:91]
	v_pk_mul_f32 v[22:23], v[22:23], v[94:95]
	v_pk_mul_f32 v[18:19], v[18:19], v[180:181]
	v_pk_mul_f32 v[16:17], v[16:17], v[88:89]
	v_pk_mul_f32 v[12:13], v[12:13], v[92:93]
	v_pk_mul_f32 v[8:9], v[8:9], v[96:97]
	v_pk_mul_f32 v[4:5], v[4:5], v[182:183]
	v_pk_mul_f32 v[14:15], v[14:15], v[86:87]
	v_pk_mul_f32 v[10:11], v[10:11], v[90:91]
	v_pk_mul_f32 v[6:7], v[6:7], v[94:95]
	v_pk_mul_f32 v[2:3], v[2:3], v[180:181]
.LBB0_1384:
	s_waitcnt vmcnt(0)
	s_barrier
	v_add_f32_e32 v179, v83, v84
	v_fmac_f32_e32 v179, v178, v82
	v_add_u32_e32 v178, s53, v194
	ds_read_b64_tr_b16 v[82:83], v178 offset:0
	ds_read_b64_tr_b16 v[84:85], v178 offset:0x800
	ds_read_b64_tr_b16 v[86:87], v178 offset:0x1000
	ds_read_b64_tr_b16 v[88:89], v178 offset:0x1800
	ds_read_b64_tr_b16 v[90:91], v178 offset:0x2000
	ds_read_b64_tr_b16 v[92:93], v178 offset:0x2800
	ds_read_b64_tr_b16 v[94:95], v178 offset:0x3000
	ds_read_b64_tr_b16 v[96:97], v178 offset:0x3800
	s_waitcnt lgkmcnt(0)
	s_nop 0
	v_mfma_f32_32x32x16_bf16 v[34:49], v[66:69], v[82:85], v[34:49]
	v_mfma_f32_32x32x16_bf16 v[34:49], v[70:73], v[86:89], v[34:49]
	v_mfma_f32_32x32x16_bf16 v[34:49], v[74:77], v[90:93], v[34:49]
	v_mfma_f32_32x32x16_bf16 v[34:49], v[78:81], v[94:97], v[34:49]
	s_cmp_lg_u32 s101, 0
	s_cbranch_scc0 .Lmla_nv0
	v_lshl_add_u64 v[230:231], v[228:229], 0, s[38:39]
	s_mov_b32 m0, s100
	v_lshl_add_u64 v[228:229], v[228:229], 0, s[40:41]
	global_load_lds_dwordx4 v[230:231], off
.Lmla_nv0:
	ds_read_b64_tr_b16 v[82:83], v178 offset:0x200
	ds_read_b64_tr_b16 v[84:85], v178 offset:0xa00
	ds_read_b64_tr_b16 v[86:87], v178 offset:0x1200
	ds_read_b64_tr_b16 v[88:89], v178 offset:0x1a00
	ds_read_b64_tr_b16 v[90:91], v178 offset:0x2200
	ds_read_b64_tr_b16 v[92:93], v178 offset:0x2a00
	ds_read_b64_tr_b16 v[94:95], v178 offset:0x3200
	ds_read_b64_tr_b16 v[96:97], v178 offset:0x3a00
	s_waitcnt lgkmcnt(0)
	s_nop 0
	v_mfma_f32_32x32x16_bf16 v[50:65], v[66:69], v[82:85], v[50:65]
	v_mfma_f32_32x32x16_bf16 v[50:65], v[70:73], v[86:89], v[50:65]
	v_mfma_f32_32x32x16_bf16 v[50:65], v[74:77], v[90:93], v[50:65]
	v_mfma_f32_32x32x16_bf16 v[50:65], v[78:81], v[94:97], v[50:65]
	s_cmp_lg_u32 s101, 0
	s_cbranch_scc0 .Lmla_nv1
	s_add_i32 m0, s100, 0x400
	s_nop 0
	global_load_lds_dwordx4 v[228:229], off
.Lmla_nv1:
	ds_read_b64_tr_b16 v[82:83], v178 offset:0x400
	ds_read_b64_tr_b16 v[84:85], v178 offset:0xc00
	ds_read_b64_tr_b16 v[86:87], v178 offset:0x1400
	ds_read_b64_tr_b16 v[88:89], v178 offset:0x1c00
	ds_read_b64_tr_b16 v[90:91], v178 offset:0x2400
	ds_read_b64_tr_b16 v[92:93], v178 offset:0x2c00
	ds_read_b64_tr_b16 v[94:95], v178 offset:0x3400
	ds_read_b64_tr_b16 v[96:97], v178 offset:0x3c00
	s_waitcnt lgkmcnt(0)
	s_nop 0
	v_mfma_f32_32x32x16_bf16 v[18:33], v[66:69], v[82:85], v[18:33]
	v_mfma_f32_32x32x16_bf16 v[18:33], v[70:73], v[86:89], v[18:33]
	v_mfma_f32_32x32x16_bf16 v[18:33], v[74:77], v[90:93], v[18:33]
	v_mfma_f32_32x32x16_bf16 v[18:33], v[78:81], v[94:97], v[18:33]
	ds_read_b64_tr_b16 v[82:83], v178 offset:0x600
	ds_read_b64_tr_b16 v[84:85], v178 offset:0xe00
	ds_read_b64_tr_b16 v[86:87], v178 offset:0x1600
	ds_read_b64_tr_b16 v[88:89], v178 offset:0x1e00
	ds_read_b64_tr_b16 v[90:91], v178 offset:0x2600
	ds_read_b64_tr_b16 v[92:93], v178 offset:0x2e00
	ds_read_b64_tr_b16 v[94:95], v178 offset:0x3600
	ds_read_b64_tr_b16 v[96:97], v178 offset:0x3e00
	s_waitcnt lgkmcnt(0)
	s_nop 0
	v_mfma_f32_32x32x16_bf16 v[2:17], v[66:69], v[82:85], v[2:17]
	v_mfma_f32_32x32x16_bf16 v[2:17], v[70:73], v[86:89], v[2:17]
	v_mfma_f32_32x32x16_bf16 v[2:17], v[74:77], v[90:93], v[2:17]
	v_mfma_f32_32x32x16_bf16 v[2:17], v[78:81], v[94:97], v[2:17]
	v_mov_b32_e32 v178, v179
	s_branch .LBB0_1385
.Lmla_inact:
	s_cmp_lt_u32 s52, s50
	s_cselect_b32 s101, 1, 0
	s_cbranch_scc0 .Lmla_in1
	s_lshl_b64 s[98:99], s[10:11], 12
	s_add_u32 s98, s44, s98
	s_addc_u32 s99, s45, s99
	s_lshl_b32 s100, s46, 14
	s_xor_b32 s100, s100, 0x4000
	s_add_i32 s100, s48, s100
	s_add_i32 m0, s100, 0x8000
	v_lshl_add_u64 v[228:229], v[146:147], 1, s[98:99]
	global_load_lds_dwordx4 v176, s[98:99]
	s_add_i32 m0, s100, 0x8400
	s_nop 0
	global_load_lds_dwordx4 v177, s[98:99]
	s_lshl_b64 s[98:99], s[10:11], 7
	s_lshl_b32 m0, s46, 13
	v_lshl_add_u64 v[232:233], v[148:149], 0, s[98:99]
	s_xor_b32 m0, m0, 0x2000
	s_add_i32 m0, s49, m0
	s_nop 0
	global_load_lds_dwordx4 v[232:233], off
.Lmla_in1:
	s_waitcnt vmcnt(0)
	s_barrier
	s_cmp_lg_u32 s101, 0
	s_cbranch_scc0 .LBB0_1385
	v_lshl_add_u64 v[230:231], v[228:229], 0, s[38:39]
	s_mov_b32 m0, s100
	v_lshl_add_u64 v[228:229], v[228:229], 0, s[40:41]
	global_load_lds_dwordx4 v[230:231], off
	s_add_i32 m0, s100, 0x400
	s_nop 0
	global_load_lds_dwordx4 v[228:229], off

; template <bool MLA>
; __device__ __forceinline__ void attn_unit(char* lds, int h, int qb, const bf16_t* Qp, int ldq, const bf16_t* Kp, int ldk, const bf16_t* KRp, const bf16_t* Vp, int ldv,
;                                           unsigned char* Op, int ldo, const float* KMp, const float* rel_bias) {
;     ...
;               for (int d0 = 0; d0 < 8; ++d0) { const char* ap = kn + kan[d0 & 3] + (d0 >> 2) * 128;
;                   const bf16x8 a0 = *(const bf16x8*)ap, a1 = *(const bf16x8*)(ap + 32 * 256);
;                   p0 = __builtin_amdgcn_mfma_f32_32x32x16_bf16(a0, qr[d0], p0, 0, 0, 0);
;                   p1 = __builtin_amdgcn_mfma_f32_32x32x16_bf16(a1, qr[d0], p1, 0, 0, 0); }
;               if constexpr (MLA) {
; #pragma unroll
;                   for (int d0 = 8; d0 < 12; ++d0) { const char* ap = kr + kar[d0 & 3];
;                       const bf16x8 a0 = *(const bf16x8*)ap, a1 = *(const bf16x8*)(ap + 32 * 128);
;                       p0 = __builtin_amdgcn_mfma_f32_32x32x16_bf16(a0, qr[d0], p0, 0, 0, 0);
;                       p1 = __builtin_amdgcn_mfma_f32_32x32x16_bf16(a1, qr[d0], p1, 0, 0, 0); } } }
;             const int dq = qpos - kb - 4 * hi;
;             if constexpr (MLA) {
;                 if (kb + 63 > qlo) {
; #pragma unroll
;                     for (int r = 0; r < 16; ++r) { const int d0 = dq - CROWC(r); if (d0 < 0) p0[r] = NEG; if (d0 < 32) p1[r] = NEG; } }
.Lmla_nk0:
	ds_read_b128 v[66:69], v70 offset:40960
	ds_read_b128 v[196:199], v70 offset:41088
	ds_read_b128 v[200:203], v179 offset:32768
	ds_read_b128 v[204:207], v179 offset:32896
	s_waitcnt lgkmcnt(0)
	v_mfma_f32_32x32x16_bf16 v[66:81], v[66:69], v[98:101], 0
	v_mfma_f32_32x32x16_bf16 v[82:97], v[200:203], v[102:105], v[82:97]
	s_cmp_lg_u32 s101, 0
	s_cbranch_scc0 .Lmla_nk1
	s_add_i32 m0, s100, 0x8400
	s_nop 0
	global_load_lds_dwordx4 v177, s[98:99]
.Lmla_nk1:
	ds_read_b128 v[200:203], v179 offset:40960
	ds_read_b128 v[208:211], v179 offset:41088
	v_add3_u32 v179, s22, v156, v153
	s_waitcnt lgkmcnt(0)
	v_mfma_f32_32x32x16_bf16 v[66:81], v[200:203], v[102:105], v[66:81]
	s_cmp_lg_u32 s101, 0
	s_cbranch_scc0 .Lmla_nk2
	s_lshl_b64 s[98:99], s[10:11], 7
	s_lshl_b32 m0, s46, 13
	v_lshl_add_u64 v[232:233], v[148:149], 0, s[98:99]
	s_xor_b32 m0, m0, 0x2000
	s_add_i32 m0, s49, m0
	s_nop 0
	global_load_lds_dwordx4 v[232:233], off
.Lmla_nk2:
	ds_read_b128 v[200:203], v179 offset:32768
	ds_read_b128 v[212:215], v179 offset:32896
	s_waitcnt lgkmcnt(0)
	v_mfma_f32_32x32x16_bf16 v[82:97], v[200:203], v[106:109], v[82:97]
	ds_read_b128 v[200:203], v179 offset:40960
	ds_read_b128 v[216:219], v179 offset:41088
	v_add3_u32 v179, s22, v157, v153
	s_sub_i32 s22, s22, s23
	s_waitcnt lgkmcnt(0)
	v_mfma_f32_32x32x16_bf16 v[66:81], v[200:203], v[106:109], v[66:81]
	ds_read_b128 v[200:203], v179 offset:32768
	ds_read_b128 v[220:223], v179 offset:32896
	s_waitcnt lgkmcnt(0)
	v_mfma_f32_32x32x16_bf16 v[82:97], v[200:203], v[110:113], v[82:97]
	ds_read_b128 v[200:203], v179 offset:40960
	ds_read_b128 v[224:227], v179 offset:41088
	v_add3_u32 v179, s22, v154, v159
	s_waitcnt lgkmcnt(0)
	v_mfma_f32_32x32x16_bf16 v[66:81], v[200:203], v[110:113], v[66:81]
	v_mfma_f32_32x32x16_bf16 v[82:97], v[180:183], v[114:117], v[82:97]
	v_mfma_f32_32x32x16_bf16 v[66:81], v[196:199], v[114:117], v[66:81]
	ds_read_b128 v[180:183], v179
	ds_read_b128 v[196:199], v179 offset:4096
	v_add3_u32 v179, s22, v155, v159
	v_mfma_f32_32x32x16_bf16 v[82:97], v[204:207], v[118:121], v[82:97]
	v_mfma_f32_32x32x16_bf16 v[66:81], v[208:211], v[118:121], v[66:81]
	v_mfma_f32_32x32x16_bf16 v[82:97], v[212:215], v[122:125], v[82:97]
	v_mfma_f32_32x32x16_bf16 v[66:81], v[216:219], v[122:125], v[66:81]
	v_mfma_f32_32x32x16_bf16 v[82:97], v[220:223], v[126:129], v[82:97]
	v_mfma_f32_32x32x16_bf16 v[66:81], v[224:227], v[126:129], v[66:81]
	s_waitcnt lgkmcnt(0)
	v_mfma_f32_32x32x16_bf16 v[82:97], v[180:183], v[130:133], v[82:97]
	v_mfma_f32_32x32x16_bf16 v[66:81], v[196:199], v[130:133], v[66:81]
	ds_read_b128 v[180:183], v179
	ds_read_b128 v[196:199], v179 offset:4096
	v_add3_u32 v179, s22, v156, v159
	s_waitcnt lgkmcnt(0)
	v_mfma_f32_32x32x16_bf16 v[82:97], v[180:183], v[134:137], v[82:97]
	v_mfma_f32_32x32x16_bf16 v[66:81], v[196:199], v[134:137], v[66:81]
	ds_read_b128 v[180:183], v179
	ds_read_b128 v[196:199], v179 offset:4096
	v_add3_u32 v179, s22, v157, v159
	s_add_i32 s22, s10, -1
	s_cmp_le_u32 s22, s42
	s_waitcnt lgkmcnt(0)
	v_mfma_f32_32x32x16_bf16 v[82:97], v[180:183], v[138:141], v[82:97]
	v_mfma_f32_32x32x16_bf16 v[66:81], v[196:199], v[138:141], v[66:81]
	ds_read_b128 v[180:183], v179
	ds_read_b128 v[196:199], v179 offset:4096
	s_waitcnt lgkmcnt(0)
	v_mfma_f32_32x32x16_bf16 v[82:97], v[180:183], v[142:145], v[82:97]
	v_mfma_f32_32x32x16_bf16 v[66:81], v[196:199], v[142:145], v[66:81]
	s_cbranch_scc1 .LBB0_1391
	v_add_u32_e32 v179, 27, v174
	v_cmp_lt_i32_e32 vcc, -1, v179
	s_nop 7
	v_cndmask_b32_e32 v82, v163, v82, vcc
	v_cmp_lt_i32_e32 vcc, 31, v179
	v_add_u32_e32 v179, 26, v174
	s_nop 0
	v_cndmask_b32_e32 v66, v163, v66, vcc
	v_cmp_lt_i32_e32 vcc, -1, v179
	s_nop 1
	v_cndmask_b32_e32 v83, v163, v83, vcc
	v_cmp_lt_i32_e32 vcc, 31, v179
	v_add_u32_e32 v179, 25, v174
	s_nop 0
	v_cndmask_b32_e32 v67, v163, v67, vcc
	v_cmp_lt_i32_e32 vcc, -1, v179
	s_nop 1
	v_cndmask_b32_e32 v84, v163, v84, vcc
	v_cmp_lt_i32_e32 vcc, 31, v179
	v_add_u32_e32 v179, 24, v174
	s_nop 0
	v_cndmask_b32_e32 v68, v163, v68, vcc
	v_cmp_lt_i32_e32 vcc, -1, v179
	s_nop 1
	v_cndmask_b32_e32 v85, v163, v85, vcc
	v_cmp_lt_i32_e32 vcc, 31, v179
	v_add_u32_e32 v179, 19, v174
	s_nop 0
	v_cndmask_b32_e32 v69, v163, v69, vcc
	v_cmp_lt_i32_e32 vcc, -1, v179
	s_nop 1
	v_cndmask_b32_e32 v86, v163, v86, vcc
	v_cmp_lt_i32_e32 vcc, 31, v179
	v_add_u32_e32 v179, 18, v174
	s_nop 0
	v_cndmask_b32_e32 v70, v163, v70, vcc
	v_cmp_lt_i32_e32 vcc, -1, v179
	s_nop 1
	v_cndmask_b32_e32 v87, v163, v87, vcc
	v_cmp_lt_i32_e32 vcc, 31, v179
	v_add_u32_e32 v179, 17, v174
	s_nop 0
	v_cndmask_b32_e32 v71, v163, v71, vcc
	v_cmp_lt_i32_e32 vcc, -1, v179
	s_nop 1
	v_cndmask_b32_e32 v88, v163, v88, vcc
	v_cmp_lt_i32_e32 vcc, 31, v179
	v_add_u32_e32 v179, 16, v174
	s_nop 0
	v_cndmask_b32_e32 v72, v163, v72, vcc
	v_cmp_lt_i32_e32 vcc, -1, v179
	s_nop 1
	v_cndmask_b32_e32 v89, v163, v89, vcc
	v_cmp_lt_i32_e32 vcc, 31, v179
	v_add_u32_e32 v179, 11, v174
	s_nop 0
	v_cndmask_b32_e32 v73, v163, v73, vcc
	v_cmp_lt_i32_e32 vcc, -1, v179
	s_nop 1
	v_cndmask_b32_e32 v90, v163, v90, vcc
	v_cmp_lt_i32_e32 vcc, 31, v179
	v_add_u32_e32 v179, 10, v174
	s_nop 0
	v_cndmask_b32_e32 v74, v163, v74, vcc
	v_cmp_lt_i32_e32 vcc, -1, v179
	s_nop 1
	v_cndmask_b32_e32 v91, v163, v91, vcc
	v_cmp_lt_i32_e32 vcc, 31, v179
	v_add_u32_e32 v179, 9, v174
	s_nop 0
	v_cndmask_b32_e32 v75, v163, v75, vcc
	v_cmp_lt_i32_e32 vcc, -1, v179
	s_nop 1
	v_cndmask_b32_e32 v92, v163, v92, vcc
	v_cmp_lt_i32_e32 vcc, 31, v179
	v_add_u32_e32 v179, 8, v174
	s_nop 0
	v_cndmask_b32_e32 v76, v163, v76, vcc
	v_cmp_lt_i32_e32 vcc, -1, v179
	s_nop 1
	v_cndmask_b32_e32 v93, v163, v93, vcc
	v_cmp_lt_i32_e32 vcc, 31, v179
	v_add_u32_e32 v179, 3, v174
	s_nop 0
	v_cndmask_b32_e32 v77, v163, v77, vcc
	v_cmp_lt_i32_e32 vcc, -1, v179
	s_nop 1
	v_cndmask_b32_e32 v94, v163, v94, vcc
	v_cmp_lt_i32_e32 vcc, 31, v179
	v_add_u32_e32 v179, 2, v174
	s_nop 0
	v_cndmask_b32_e32 v78, v163, v78, vcc
	v_cmp_lt_i32_e32 vcc, -1, v179
	s_nop 1
	v_cndmask_b32_e32 v95, v163, v95, vcc
	v_cmp_lt_i32_e32 vcc, 31, v179
	v_add_u32_e32 v179, 1, v174
	s_nop 0
	v_cndmask_b32_e32 v79, v163, v79, vcc
	v_cmp_lt_i32_e32 vcc, -1, v179
	s_nop 1
	v_cndmask_b32_e32 v96, v163, v96, vcc
	v_cmp_lt_i32_e32 vcc, 31, v179
	s_nop 1
	v_cndmask_b32_e32 v80, v163, v80, vcc
	v_cmp_lt_i32_e32 vcc, -1, v174
	s_nop 1
	v_cndmask_b32_e32 v97, v163, v97, vcc
	v_cmp_lt_i32_e32 vcc, 31, v174
	s_nop 1
	v_cndmask_b32_e32 v81, v163, v81, vcc

; #define LDS_WAIT() asm volatile("s_waitcnt lgkmcnt(0)" ::: "memory")
; #define VM_WAIT() asm volatile("s_waitcnt vmcnt(0)" ::: "memory")
; template <bool MLA>
; __device__ __forceinline__ void attn_unit(char* lds, int h, int qb, const bf16_t* Qp, int ldq, const bf16_t* Kp, int ldk, const bf16_t* KRp, const bf16_t* Vp, int ldv,
;                                           unsigned char* Op, int ldo, const float* KMp, const float* rel_bias) {
;     ...
;         VM_WAIT();
;         __syncthreads();
;     }
;     ...
;     if (hi == 0) li_l[r32] = l_reg; LDS_WAIT();
.LBB0_1394:
	v_readfirstlane_b32 s98, v0
	s_nop 3
	s_bitcmp1_b32 s98, 8
	s_cbranch_scc1 .Lmla_noxe
	s_barrier
